# fft_a twiddle gathers de-waterfalled: 16 loads per k-block hoisted above the MFMAs, counted vmcnt(15) waits, on top of v4_mout
# speedup vs baseline: 1.0046x; 1.0032x over previous
.LBB0_865:
	ds_read_b128 v[20:23], v145 offset:34816
	ds_read_b128 v[4:7], v145
	ds_read_b128 v[146:149], v145 offset:32
	ds_read_b128 v[150:153], v145 offset:34848
	v_lshl_add_u64 v[106:107], v[2:3], 3, s[2:3]
	global_load_dwordx2 v[106:107], v[106:107], off
	v_add_u32_e32 v182, v108, v2
	v_mov_b32_e32 v183, v3
	v_lshl_add_u64 v[182:183], v[182:183], 3, s[2:3]
	global_load_dwordx2 v[182:183], v[182:183], off
	v_add_u32_e32 v184, v112, v2
	v_mov_b32_e32 v185, v3
	v_lshl_add_u64 v[184:185], v[184:185], 3, s[2:3]
	global_load_dwordx2 v[184:185], v[184:185], off
	v_add_u32_e32 v186, v113, v2
	v_mov_b32_e32 v187, v3
	v_lshl_add_u64 v[186:187], v[186:187], 3, s[2:3]
	global_load_dwordx2 v[186:187], v[186:187], off
	v_add_u32_e32 v188, v114, v2
	v_mov_b32_e32 v189, v3
	v_lshl_add_u64 v[188:189], v[188:189], 3, s[2:3]
	global_load_dwordx2 v[188:189], v[188:189], off
	v_add_u32_e32 v190, v115, v2
	v_mov_b32_e32 v191, v3
	v_lshl_add_u64 v[190:191], v[190:191], 3, s[2:3]
	global_load_dwordx2 v[190:191], v[190:191], off
	v_add_u32_e32 v192, v116, v2
	v_mov_b32_e32 v193, v3
	v_lshl_add_u64 v[192:193], v[192:193], 3, s[2:3]
	global_load_dwordx2 v[192:193], v[192:193], off
	v_add_u32_e32 v194, v117, v2
	v_mov_b32_e32 v195, v3
	v_lshl_add_u64 v[194:195], v[194:195], 3, s[2:3]
	global_load_dwordx2 v[194:195], v[194:195], off
	v_add_u32_e32 v196, v118, v2
	v_mov_b32_e32 v197, v3
	v_lshl_add_u64 v[196:197], v[196:197], 3, s[2:3]
	global_load_dwordx2 v[196:197], v[196:197], off
	v_add_u32_e32 v198, v119, v2
	v_mov_b32_e32 v199, v3
	v_lshl_add_u64 v[198:199], v[198:199], 3, s[2:3]
	global_load_dwordx2 v[198:199], v[198:199], off
	v_add_u32_e32 v214, v120, v2
	v_mov_b32_e32 v215, v3
	v_lshl_add_u64 v[214:215], v[214:215], 3, s[2:3]
	global_load_dwordx2 v[214:215], v[214:215], off
	v_add_u32_e32 v216, v121, v2
	v_mov_b32_e32 v217, v3
	v_lshl_add_u64 v[216:217], v[216:217], 3, s[2:3]
	global_load_dwordx2 v[216:217], v[216:217], off
	v_add_u32_e32 v218, v122, v2
	v_mov_b32_e32 v219, v3
	v_lshl_add_u64 v[218:219], v[218:219], 3, s[2:3]
	global_load_dwordx2 v[218:219], v[218:219], off
	v_add_u32_e32 v220, v123, v2
	v_mov_b32_e32 v221, v3
	v_lshl_add_u64 v[220:221], v[220:221], 3, s[2:3]
	global_load_dwordx2 v[220:221], v[220:221], off
	v_add_u32_e32 v222, v124, v2
	v_mov_b32_e32 v223, v3
	v_lshl_add_u64 v[222:223], v[222:223], 3, s[2:3]
	global_load_dwordx2 v[222:223], v[222:223], off
	v_add_u32_e32 v228, v125, v2
	v_mov_b32_e32 v229, v3
	v_lshl_add_u64 v[228:229], v[228:229], 3, s[2:3]
	global_load_dwordx2 v[228:229], v[228:229], off
	s_waitcnt lgkmcnt(3)
	v_mfma_f32_32x32x16_bf16 v[20:35], v[20:23], v[36:39], 0
	s_waitcnt lgkmcnt(2)
	v_mfma_f32_32x32x16_bf16 v[4:19], v[4:7], v[36:39], 0
	s_waitcnt lgkmcnt(1)
	v_mfma_f32_32x32x16_bf16 v[4:19], v[146:149], v[40:43], v[4:19]
	s_waitcnt lgkmcnt(0)
	v_mfma_f32_32x32x16_bf16 v[20:35], v[150:153], v[40:43], v[20:35]
	ds_read_b128 v[146:149], v145 offset:64
	ds_read_b128 v[150:153], v145 offset:34880
	s_waitcnt lgkmcnt(1)
	v_mfma_f32_32x32x16_bf16 v[4:19], v[146:149], v[44:47], v[4:19]
	s_waitcnt lgkmcnt(0)
	v_mfma_f32_32x32x16_bf16 v[20:35], v[150:153], v[44:47], v[20:35]
	ds_read_b128 v[146:149], v145 offset:96
	ds_read_b128 v[150:153], v145 offset:34912
	s_waitcnt lgkmcnt(1)
	v_mfma_f32_32x32x16_bf16 v[4:19], v[146:149], v[48:51], v[4:19]
	s_waitcnt lgkmcnt(0)
	v_mfma_f32_32x32x16_bf16 v[20:35], v[150:153], v[48:51], v[20:35]
	ds_read_b128 v[146:149], v145 offset:128
	ds_read_b128 v[150:153], v145 offset:34944
	s_waitcnt lgkmcnt(1)
	v_mfma_f32_32x32x16_bf16 v[4:19], v[146:149], v[52:55], v[4:19]
	s_waitcnt lgkmcnt(0)
	v_mfma_f32_32x32x16_bf16 v[20:35], v[150:153], v[52:55], v[20:35]
	ds_read_b128 v[146:149], v145 offset:160
	ds_read_b128 v[150:153], v145 offset:34976
	s_waitcnt lgkmcnt(1)
	v_mfma_f32_32x32x16_bf16 v[4:19], v[146:149], v[56:59], v[4:19]
	s_waitcnt lgkmcnt(0)
	v_mfma_f32_32x32x16_bf16 v[20:35], v[150:153], v[56:59], v[20:35]
	ds_read_b128 v[146:149], v145 offset:192
	ds_read_b128 v[150:153], v145 offset:35008
	s_waitcnt lgkmcnt(1)
	v_mfma_f32_32x32x16_bf16 v[4:19], v[146:149], v[60:63], v[4:19]
	s_waitcnt lgkmcnt(0)
	v_mfma_f32_32x32x16_bf16 v[20:35], v[150:153], v[60:63], v[20:35]
	ds_read_b128 v[146:149], v145 offset:224
	ds_read_b128 v[150:153], v145 offset:35040
	v_add_u32_e32 v145, 0x2200, v145
	s_waitcnt lgkmcnt(1)
	v_mfma_f32_32x32x16_bf16 v[4:19], v[146:149], v[64:67], v[4:19]
	s_waitcnt lgkmcnt(0)
	v_mfma_f32_32x32x16_bf16 v[20:35], v[150:153], v[64:67], v[20:35]
	s_waitcnt vmcnt(15)
	s_nop 8
	v_mul_f32_e64 v146, v4, v106
	v_mul_f32_e64 v147, v4, v107
	v_pk_fma_f32 v[148:149], v[20:21], v[106:107], v[146:147] op_sel:[0,1,0] op_sel_hi:[1,0,1]
	v_pk_fma_f32 v[106:107], v[20:21], v[106:107], v[146:147] op_sel:[0,1,0] op_sel_hi:[0,0,1] neg_lo:[0,0,1] neg_hi:[0,0,1]
	v_add_u32_e32 v106, s0, v144
	v_cvt_pk_bf16_f32 v148, v148, v107
	v_ashrrev_i32_e32 v107, 31, v106
	v_lshlrev_b64 v[146:147], 16, v[106:107]
	v_lshl_add_u64 v[146:147], v[104:105], 0, v[146:147]
	global_store_dword v[146:147], v148, off
	s_add_i32 s0, s0, 32
	s_cmpk_lg_i32 s0, 0x80
	s_waitcnt vmcnt(15)
	v_pk_mul_f32 v[4:5], v[4:5], v[182:183] op_sel:[1,0]
	s_nop 0
	v_pk_fma_f32 v[148:149], v[20:21], v[182:183], v[4:5] op_sel:[1,1,0] op_sel_hi:[1,0,1]
	v_pk_fma_f32 v[4:5], v[20:21], v[182:183], v[4:5] op_sel:[1,1,0] op_sel_hi:[1,0,1] neg_lo:[0,0,1] neg_hi:[0,0,1]
	s_nop 0
	v_add_u32_e32 v4, 1, v106
	v_cvt_pk_bf16_f32 v20, v148, v5
	v_ashrrev_i32_e32 v5, 31, v4
	v_lshlrev_b64 v[4:5], 16, v[4:5]
	v_lshl_add_u64 v[4:5], v[104:105], 0, v[4:5]
	global_store_dword v[4:5], v20, off
	s_waitcnt vmcnt(15)
	v_pk_mul_f32 v[20:21], v[6:7], v[184:185] op_sel_hi:[0,1]
	v_pk_fma_f32 v[146:147], v[22:23], v[184:185], v[20:21] op_sel:[0,1,0] op_sel_hi:[1,0,1]
	v_pk_fma_f32 v[4:5], v[22:23], v[184:185], v[20:21] op_sel:[0,1,0] op_sel_hi:[0,0,1] neg_lo:[0,0,1] neg_hi:[0,0,1]
	v_add_u32_e32 v4, 2, v106
	v_cvt_pk_bf16_f32 v6, v146, v5
	v_ashrrev_i32_e32 v5, 31, v4
	v_lshlrev_b64 v[4:5], 16, v[4:5]
	v_lshl_add_u64 v[4:5], v[104:105], 0, v[4:5]
	global_store_dword v[4:5], v6, off
	v_mov_b32_e32 v20, v7
	v_mov_b32_e32 v6, v23
	s_waitcnt vmcnt(15)
	v_pk_mul_f32 v[20:21], v[20:21], v[186:187] op_sel_hi:[0,1]
	v_pk_fma_f32 v[22:23], v[6:7], v[186:187], v[20:21] op_sel:[0,1,0] op_sel_hi:[0,0,1]
	v_pk_fma_f32 v[4:5], v[6:7], v[186:187], v[20:21] op_sel:[0,1,0] op_sel_hi:[0,0,1] neg_lo:[0,0,1] neg_hi:[0,0,1]
	v_add_u32_e32 v4, 3, v106
	v_cvt_pk_bf16_f32 v6, v22, v5
	v_ashrrev_i32_e32 v5, 31, v4
	v_lshlrev_b64 v[4:5], 16, v[4:5]
	v_lshl_add_u64 v[4:5], v[104:105], 0, v[4:5]
	global_store_dword v[4:5], v6, off
	s_waitcnt vmcnt(15)
	v_pk_mul_f32 v[6:7], v[8:9], v[188:189] op_sel_hi:[0,1]
	v_pk_fma_f32 v[20:21], v[24:25], v[188:189], v[6:7] op_sel:[0,1,0] op_sel_hi:[1,0,1]
	v_pk_fma_f32 v[4:5], v[24:25], v[188:189], v[6:7] op_sel:[0,1,0] op_sel_hi:[0,0,1] neg_lo:[0,0,1] neg_hi:[0,0,1]
	v_add_u32_e32 v4, 8, v106
	v_cvt_pk_bf16_f32 v6, v20, v5
	v_ashrrev_i32_e32 v5, 31, v4
	v_lshlrev_b64 v[4:5], 16, v[4:5]
	v_lshl_add_u64 v[4:5], v[104:105], 0, v[4:5]
	global_store_dword v[4:5], v6, off
	v_mov_b32_e32 v8, v9
	v_mov_b32_e32 v6, v25
	s_waitcnt vmcnt(15)
	v_pk_mul_f32 v[8:9], v[8:9], v[190:191] op_sel_hi:[0,1]
	v_pk_fma_f32 v[20:21], v[6:7], v[190:191], v[8:9] op_sel:[0,1,0] op_sel_hi:[0,0,1]
	v_pk_fma_f32 v[4:5], v[6:7], v[190:191], v[8:9] op_sel:[0,1,0] op_sel_hi:[0,0,1] neg_lo:[0,0,1] neg_hi:[0,0,1]
	v_add_u32_e32 v4, 9, v106
	v_cvt_pk_bf16_f32 v6, v20, v5
	v_ashrrev_i32_e32 v5, 31, v4
	v_lshlrev_b64 v[4:5], 16, v[4:5]
	v_lshl_add_u64 v[4:5], v[104:105], 0, v[4:5]
	global_store_dword v[4:5], v6, off
	s_waitcnt vmcnt(15)
	v_pk_mul_f32 v[6:7], v[10:11], v[192:193] op_sel_hi:[0,1]
	v_pk_fma_f32 v[8:9], v[26:27], v[192:193], v[6:7] op_sel:[0,1,0] op_sel_hi:[1,0,1]
	v_pk_fma_f32 v[4:5], v[26:27], v[192:193], v[6:7] op_sel:[0,1,0] op_sel_hi:[0,0,1] neg_lo:[0,0,1] neg_hi:[0,0,1]
	v_add_u32_e32 v4, 10, v106
	v_cvt_pk_bf16_f32 v6, v8, v5
	v_ashrrev_i32_e32 v5, 31, v4
	v_lshlrev_b64 v[4:5], 16, v[4:5]
	v_lshl_add_u64 v[4:5], v[104:105], 0, v[4:5]
	global_store_dword v[4:5], v6, off
	v_mov_b32_e32 v8, v11
	v_mov_b32_e32 v6, v27
	s_waitcnt vmcnt(15)
	v_pk_mul_f32 v[8:9], v[8:9], v[194:195] op_sel_hi:[0,1]
	v_pk_fma_f32 v[10:11], v[6:7], v[194:195], v[8:9] op_sel:[0,1,0] op_sel_hi:[0,0,1]
	v_pk_fma_f32 v[4:5], v[6:7], v[194:195], v[8:9] op_sel:[0,1,0] op_sel_hi:[0,0,1] neg_lo:[0,0,1] neg_hi:[0,0,1]
	v_add_u32_e32 v4, 11, v106
	v_cvt_pk_bf16_f32 v6, v10, v5
	v_ashrrev_i32_e32 v5, 31, v4
	v_lshlrev_b64 v[4:5], 16, v[4:5]
	v_lshl_add_u64 v[4:5], v[104:105], 0, v[4:5]
	global_store_dword v[4:5], v6, off
	s_waitcnt vmcnt(15)
	v_pk_mul_f32 v[6:7], v[12:13], v[196:197] op_sel_hi:[0,1]
	v_pk_fma_f32 v[8:9], v[28:29], v[196:197], v[6:7] op_sel:[0,1,0] op_sel_hi:[1,0,1]
	v_pk_fma_f32 v[4:5], v[28:29], v[196:197], v[6:7] op_sel:[0,1,0] op_sel_hi:[0,0,1] neg_lo:[0,0,1] neg_hi:[0,0,1]
	v_add_u32_e32 v4, 16, v106
	v_cvt_pk_bf16_f32 v6, v8, v5
	v_ashrrev_i32_e32 v5, 31, v4
	v_lshlrev_b64 v[4:5], 16, v[4:5]
	v_lshl_add_u64 v[4:5], v[104:105], 0, v[4:5]
	global_store_dword v[4:5], v6, off
	v_mov_b32_e32 v8, v13
	v_mov_b32_e32 v6, v29
	s_waitcnt vmcnt(15)
	v_pk_mul_f32 v[8:9], v[8:9], v[198:199] op_sel_hi:[0,1]
	v_pk_fma_f32 v[10:11], v[6:7], v[198:199], v[8:9] op_sel:[0,1,0] op_sel_hi:[0,0,1]
	v_pk_fma_f32 v[4:5], v[6:7], v[198:199], v[8:9] op_sel:[0,1,0] op_sel_hi:[0,0,1] neg_lo:[0,0,1] neg_hi:[0,0,1]
	v_add_u32_e32 v4, 17, v106
	v_cvt_pk_bf16_f32 v6, v10, v5
	v_ashrrev_i32_e32 v5, 31, v4
	v_lshlrev_b64 v[4:5], 16, v[4:5]
	v_lshl_add_u64 v[4:5], v[104:105], 0, v[4:5]
	global_store_dword v[4:5], v6, off
	s_waitcnt vmcnt(15)
	v_pk_mul_f32 v[6:7], v[14:15], v[214:215] op_sel_hi:[0,1]
	v_pk_fma_f32 v[8:9], v[30:31], v[214:215], v[6:7] op_sel:[0,1,0] op_sel_hi:[1,0,1]
	v_pk_fma_f32 v[4:5], v[30:31], v[214:215], v[6:7] op_sel:[0,1,0] op_sel_hi:[0,0,1] neg_lo:[0,0,1] neg_hi:[0,0,1]
	v_add_u32_e32 v4, 18, v106
	v_cvt_pk_bf16_f32 v6, v8, v5
	v_ashrrev_i32_e32 v5, 31, v4
	v_lshlrev_b64 v[4:5], 16, v[4:5]
	v_lshl_add_u64 v[4:5], v[104:105], 0, v[4:5]
	global_store_dword v[4:5], v6, off
	v_mov_b32_e32 v8, v15
	v_mov_b32_e32 v6, v31
	s_waitcnt vmcnt(15)
	v_pk_mul_f32 v[8:9], v[8:9], v[216:217] op_sel_hi:[0,1]
	v_pk_fma_f32 v[10:11], v[6:7], v[216:217], v[8:9] op_sel:[0,1,0] op_sel_hi:[0,0,1]
	v_pk_fma_f32 v[4:5], v[6:7], v[216:217], v[8:9] op_sel:[0,1,0] op_sel_hi:[0,0,1] neg_lo:[0,0,1] neg_hi:[0,0,1]
	v_add_u32_e32 v4, 19, v106
	v_cvt_pk_bf16_f32 v6, v10, v5
	v_ashrrev_i32_e32 v5, 31, v4
	v_lshlrev_b64 v[4:5], 16, v[4:5]
	v_lshl_add_u64 v[4:5], v[104:105], 0, v[4:5]
	global_store_dword v[4:5], v6, off
	s_waitcnt vmcnt(15)
	v_pk_mul_f32 v[6:7], v[16:17], v[218:219] op_sel_hi:[0,1]
	v_pk_fma_f32 v[8:9], v[32:33], v[218:219], v[6:7] op_sel:[0,1,0] op_sel_hi:[1,0,1]
	v_pk_fma_f32 v[4:5], v[32:33], v[218:219], v[6:7] op_sel:[0,1,0] op_sel_hi:[0,0,1] neg_lo:[0,0,1] neg_hi:[0,0,1]
	v_add_u32_e32 v4, 24, v106
	v_cvt_pk_bf16_f32 v6, v8, v5
	v_ashrrev_i32_e32 v5, 31, v4
	v_lshlrev_b64 v[4:5], 16, v[4:5]
	v_lshl_add_u64 v[4:5], v[104:105], 0, v[4:5]
	global_store_dword v[4:5], v6, off
	v_mov_b32_e32 v8, v17
	v_mov_b32_e32 v6, v33
	s_waitcnt vmcnt(15)
	v_pk_mul_f32 v[8:9], v[8:9], v[220:221] op_sel_hi:[0,1]
	v_pk_fma_f32 v[10:11], v[6:7], v[220:221], v[8:9] op_sel:[0,1,0] op_sel_hi:[0,0,1]
	v_pk_fma_f32 v[4:5], v[6:7], v[220:221], v[8:9] op_sel:[0,1,0] op_sel_hi:[0,0,1] neg_lo:[0,0,1] neg_hi:[0,0,1]
	v_add_u32_e32 v4, 25, v106
	v_cvt_pk_bf16_f32 v6, v10, v5
	v_ashrrev_i32_e32 v5, 31, v4
	v_lshlrev_b64 v[4:5], 16, v[4:5]
	v_lshl_add_u64 v[4:5], v[104:105], 0, v[4:5]
	global_store_dword v[4:5], v6, off
	s_waitcnt vmcnt(15)
	v_pk_mul_f32 v[6:7], v[18:19], v[222:223] op_sel_hi:[0,1]
	v_pk_fma_f32 v[8:9], v[34:35], v[222:223], v[6:7] op_sel:[0,1,0] op_sel_hi:[1,0,1]
	v_pk_fma_f32 v[4:5], v[34:35], v[222:223], v[6:7] op_sel:[0,1,0] op_sel_hi:[0,0,1] neg_lo:[0,0,1] neg_hi:[0,0,1]
	v_add_u32_e32 v4, 26, v106
	v_cvt_pk_bf16_f32 v6, v8, v5
	v_ashrrev_i32_e32 v5, 31, v4
	v_lshlrev_b64 v[4:5], 16, v[4:5]
	v_lshl_add_u64 v[4:5], v[104:105], 0, v[4:5]
	global_store_dword v[4:5], v6, off
	v_mov_b32_e32 v8, v19
	v_mov_b32_e32 v6, v35
	v_add_u32_e32 v2, v2, v111
	s_waitcnt vmcnt(15)
	v_pk_mul_f32 v[8:9], v[8:9], v[228:229] op_sel_hi:[0,1]
	v_pk_fma_f32 v[10:11], v[6:7], v[228:229], v[8:9] op_sel:[0,1,0] op_sel_hi:[0,0,1]
	v_pk_fma_f32 v[4:5], v[6:7], v[228:229], v[8:9] op_sel:[0,1,0] op_sel_hi:[0,0,1] neg_lo:[0,0,1] neg_hi:[0,0,1]
	v_add_u32_e32 v4, 27, v106
	v_cvt_pk_bf16_f32 v6, v10, v5
	v_ashrrev_i32_e32 v5, 31, v4
	v_lshlrev_b64 v[4:5], 16, v[4:5]
	v_lshl_add_u64 v[4:5], v[104:105], 0, v[4:5]
	global_store_dword v[4:5], v6, off
	s_cbranch_scc1 .LBB0_865
	v_readlane_b32 s0, v254, 4
	v_readlane_b32 s1, v254, 5
	s_load_dword s0, s[0:1], 0x0
	s_waitcnt lgkmcnt(0)
	s_add_i32 s7, s0, s7
	s_cmpk_lt_i32 s7, 0x200
	s_cbranch_scc1 .LBB0_864
